# baseline (speedup 1.0000x reference)
_Z8k_expertPKDF16_S0_PKfPcPiS0_S2_S2_S2_S2_PfS5_S4_S2_S2_S2_S2_S5_S2_S2_S2_:
	s_lshl_b32 s3, s2, 2
	s_load_dwordx8 s[8:15], s[0:1], 0x88
	s_load_dwordx2 s[70:71], s[0:1], 0x0
	s_and_b32 s3, s3, 28
	s_ashr_i32 s4, s2, 6
	s_add_i32 s34, s3, s4
	s_ashr_i32 s6, s34, 1
	v_mov_b32_e32 v2, v0
	s_lshl_b32 s4, s6, 4
	s_ashr_i32 s5, s4, 31
	v_ashrrev_i32_e32 v3, 31, v2
	s_waitcnt lgkmcnt(0)
	s_load_dwordx8 s[16:23], s[14:15], 0x0
	v_lshl_add_u64 v[4:5], v[2:3], 2, s[10:11]
	s_lshl_b64 s[10:11], s[4:5], 11
	v_lshl_add_u64 v[6:7], v[4:5], 0, s[10:11]
	s_or_b32 s10, s4, 1
	s_ashr_i32 s11, s10, 31
	s_lshl_b64 s[10:11], s[10:11], 11
	v_lshl_add_u64 v[8:9], v[4:5], 0, s[10:11]
	s_or_b32 s10, s4, 2
	s_ashr_i32 s11, s10, 31
	s_lshl_b64 s[10:11], s[10:11], 11
	v_lshl_add_u64 v[10:11], v[4:5], 0, s[10:11]
	s_or_b32 s10, s4, 3
	s_ashr_i32 s11, s10, 31
	s_lshl_b64 s[10:11], s[10:11], 11
	v_lshl_add_u64 v[12:13], v[4:5], 0, s[10:11]
	s_or_b32 s10, s4, 4
	s_ashr_i32 s11, s10, 31
	s_lshl_b64 s[10:11], s[10:11], 11
	v_lshl_add_u64 v[14:15], v[4:5], 0, s[10:11]
	s_or_b32 s10, s4, 5
	s_ashr_i32 s11, s10, 31
	s_lshl_b64 s[10:11], s[10:11], 11
	v_lshl_add_u64 v[16:17], v[4:5], 0, s[10:11]
	s_or_b32 s10, s4, 6
	s_ashr_i32 s11, s10, 31
	s_lshl_b64 s[10:11], s[10:11], 11
	v_lshl_add_u64 v[18:19], v[4:5], 0, s[10:11]
	s_or_b32 s10, s4, 7
	s_ashr_i32 s11, s10, 31
	s_lshl_b64 s[10:11], s[10:11], 11
	v_lshl_add_u64 v[20:21], v[4:5], 0, s[10:11]
	s_or_b32 s10, s4, 8
	s_ashr_i32 s11, s10, 31
	s_lshl_b64 s[10:11], s[10:11], 11
	global_load_dword v1, v[6:7], off
	global_load_dword v3, v[8:9], off
	global_load_dword v22, v[10:11], off
	global_load_dword v23, v[12:13], off
	global_load_dword v24, v[14:15], off
	global_load_dword v25, v[16:17], off
	global_load_dword v26, v[18:19], off
	global_load_dword v27, v[20:21], off
	v_lshl_add_u64 v[6:7], v[4:5], 0, s[10:11]
	s_or_b32 s10, s4, 9
	s_ashr_i32 s11, s10, 31
	s_lshl_b64 s[10:11], s[10:11], 11
	v_lshl_add_u64 v[8:9], v[4:5], 0, s[10:11]
	s_or_b32 s10, s4, 10
	s_ashr_i32 s11, s10, 31
	s_lshl_b64 s[10:11], s[10:11], 11
	v_lshl_add_u64 v[10:11], v[4:5], 0, s[10:11]
	s_or_b32 s10, s4, 11
	s_ashr_i32 s11, s10, 31
	s_lshl_b64 s[10:11], s[10:11], 11
	v_lshl_add_u64 v[12:13], v[4:5], 0, s[10:11]
	s_or_b32 s10, s4, 12
	s_ashr_i32 s11, s10, 31
	s_lshl_b64 s[10:11], s[10:11], 11
	v_lshl_add_u64 v[14:15], v[4:5], 0, s[10:11]
	s_or_b32 s10, s4, 13
	s_ashr_i32 s11, s10, 31
	s_lshl_b64 s[10:11], s[10:11], 11
	v_lshl_add_u64 v[16:17], v[4:5], 0, s[10:11]
	s_or_b32 s10, s4, 14
	s_or_b32 s4, s4, 15
	s_ashr_i32 s11, s10, 31
	s_ashr_i32 s5, s4, 31
	s_lshl_b64 s[10:11], s[10:11], 11
	s_lshl_b64 s[4:5], s[4:5], 11
	v_lshl_add_u64 v[18:19], v[4:5], 0, s[10:11]
	v_lshl_add_u64 v[4:5], v[4:5], 0, s[4:5]
	global_load_dword v20, v[6:7], off
	global_load_dword v21, v[8:9], off
	global_load_dword v28, v[10:11], off
	global_load_dword v29, v[12:13], off
	global_load_dword v30, v[14:15], off
	global_load_dword v31, v[16:17], off
	global_load_dword v32, v[18:19], off
	global_load_dword v33, v[4:5], off
	v_lshlrev_b32_e32 v4, 3, v2
	v_ashrrev_i32_e32 v5, 31, v4
	v_lshl_add_u64 v[12:13], v[4:5], 2, s[12:13]
	global_load_dwordx4 v[4:7], v[12:13], off
	global_load_dwordx4 v[8:11], v[12:13], off offset:16
	v_and_b32_e32 v200, 63, v0
	v_lshrrev_b32_e32 v201, 6, v0
	v_lshlrev_b32_e32 v202, 4, v200
	v_and_b32_e32 v203, 32, v200
	v_xor_b32_e32 v202, v202, v203
	v_lshrrev_b32_e32 v203, 6, v202
	v_lshrrev_b32_e32 v204, 1, v201
	v_lshl_add_u32 v203, v204, 4, v203
	v_and_b32_e32 v204, 62, v202
	v_and_b32_e32 v205, 1, v201
	v_lshl_add_u32 v204, v205, 6, v204
	v_lshl_add_u32 v200, v203, 12, v204
	v_add_u32_e32 v201, 0x40000, v200
	s_lshl_b32 s72, s6, 22
	s_lshr_b32 s73, s2, 4
	s_and_b32 s73, s73, 3
	s_lshl_b32 s73, s73, 20
	s_add_u32 s72, s72, s73
	s_add_u32 s74, s70, s72
	s_addc_u32 s75, s71, 0
	s_add_u32 s76, s74, 0x80000
	s_addc_u32 s77, s75, 0
	v_readfirstlane_b32 s78, v0
	s_lshl_b32 s78, s78, 4
	s_mov_b32 m0, s78
	s_add_i32 s79, s78, 0x2000
	global_load_lds_dwordx4 v200, s[74:75]
	s_mov_b32 m0, s79
	s_add_i32 s79, s78, 0x4000
	global_load_lds_dwordx4 v201, s[74:75]
	s_mov_b32 m0, s79
	s_add_i32 s79, s78, 0x6000
	global_load_lds_dwordx4 v200, s[76:77]
	s_mov_b32 m0, s79
	s_nop 0
	global_load_lds_dwordx4 v201, s[76:77]
	s_add_u32 s76, s74, 0x80
	s_addc_u32 s77, s75, 0
	s_add_i32 s79, s78, 0x8000
	s_mov_b32 m0, s79
	s_add_i32 s79, s78, 0xa000
	global_load_lds_dwordx4 v200, s[76:77]
	s_mov_b32 m0, s79
	s_nop 0
	global_load_lds_dwordx4 v201, s[76:77]
	s_waitcnt vmcnt(23)
	v_add_f32_e32 v1, 0, v1
	s_waitcnt vmcnt(22)
	v_add_f32_e32 v1, v1, v3
	s_waitcnt vmcnt(21)
	v_add_f32_e32 v1, v1, v22
	s_waitcnt vmcnt(20)
	v_add_f32_e32 v1, v1, v23
	s_waitcnt vmcnt(19)
	v_add_f32_e32 v1, v1, v24
	s_waitcnt vmcnt(18)
	v_add_f32_e32 v1, v1, v25
	s_waitcnt vmcnt(17)
	v_add_f32_e32 v1, v1, v26
	s_waitcnt vmcnt(16)
	v_add_f32_e32 v1, v1, v27
	s_waitcnt vmcnt(15)
	v_add_f32_e32 v1, v1, v20
	s_waitcnt vmcnt(14)
	v_add_f32_e32 v1, v1, v21
	s_waitcnt vmcnt(13)
	v_add_f32_e32 v1, v1, v28
	s_waitcnt vmcnt(12)
	v_add_f32_e32 v1, v1, v29
	s_waitcnt vmcnt(11)
	v_add_f32_e32 v1, v1, v30
	s_waitcnt vmcnt(10)
	v_add_f32_e32 v1, v1, v31
	s_waitcnt vmcnt(9)
	v_add_f32_e32 v1, v1, v32
	s_waitcnt vmcnt(8)
	v_add_f32_e32 v1, v1, v33
	v_mul_f32_e32 v12, 0x3a800000, v1
	v_mbcnt_lo_u32_b32 v1, -1, 0
	v_mbcnt_hi_u32_b32 v3, -1, v1
	v_xor_b32_e32 v13, 32, v3
	v_lshlrev_b32_e32 v183, 2, v13
	v_xor_b32_e32 v13, 16, v3
	v_lshlrev_b32_e32 v181, 2, v13
	v_xor_b32_e32 v13, 8, v3
	v_lshlrev_b32_e32 v1, 2, v13
	v_xor_b32_e32 v13, 4, v3
	v_lshlrev_b32_e32 v180, 2, v13
	v_xor_b32_e32 v13, 2, v3
	v_lshlrev_b32_e32 v182, 2, v13
	v_xor_b32_e32 v13, 1, v3
	v_lshlrev_b32_e32 v184, 2, v13
	v_cmp_eq_u32_e32 vcc, 0, v3
	v_mov_b32_e32 v13, v12
	s_waitcnt vmcnt(6)
	v_pk_mul_f32 v[14:15], v[12:13], v[4:5]
	v_pk_mul_f32 v[16:17], v[12:13], v[6:7]
	v_pk_mul_f32 v[18:19], v[12:13], v[8:9]
	v_pk_mul_f32 v[20:21], v[12:13], v[10:11]
	v_add_f32_dpp v14, v14, v14 quad_perm:[1,0,3,2] row_mask:0xf bank_mask:0xf
	v_add_f32_dpp v15, v15, v15 quad_perm:[1,0,3,2] row_mask:0xf bank_mask:0xf
	v_add_f32_dpp v16, v16, v16 quad_perm:[1,0,3,2] row_mask:0xf bank_mask:0xf
	v_add_f32_dpp v17, v17, v17 quad_perm:[1,0,3,2] row_mask:0xf bank_mask:0xf
	v_add_f32_dpp v18, v18, v18 quad_perm:[1,0,3,2] row_mask:0xf bank_mask:0xf
	v_add_f32_dpp v19, v19, v19 quad_perm:[1,0,3,2] row_mask:0xf bank_mask:0xf
	v_add_f32_dpp v20, v20, v20 quad_perm:[1,0,3,2] row_mask:0xf bank_mask:0xf
	v_add_f32_dpp v21, v21, v21 quad_perm:[1,0,3,2] row_mask:0xf bank_mask:0xf
	v_add_f32_dpp v14, v14, v14 quad_perm:[2,3,0,1] row_mask:0xf bank_mask:0xf
	v_add_f32_dpp v15, v15, v15 quad_perm:[2,3,0,1] row_mask:0xf bank_mask:0xf
	v_add_f32_dpp v16, v16, v16 quad_perm:[2,3,0,1] row_mask:0xf bank_mask:0xf
	v_add_f32_dpp v17, v17, v17 quad_perm:[2,3,0,1] row_mask:0xf bank_mask:0xf
	v_add_f32_dpp v18, v18, v18 quad_perm:[2,3,0,1] row_mask:0xf bank_mask:0xf
	v_add_f32_dpp v19, v19, v19 quad_perm:[2,3,0,1] row_mask:0xf bank_mask:0xf
	v_add_f32_dpp v20, v20, v20 quad_perm:[2,3,0,1] row_mask:0xf bank_mask:0xf
	v_add_f32_dpp v21, v21, v21 quad_perm:[2,3,0,1] row_mask:0xf bank_mask:0xf
	v_add_f32_dpp v14, v14, v14 row_half_mirror row_mask:0xf bank_mask:0xf
	v_add_f32_dpp v15, v15, v15 row_half_mirror row_mask:0xf bank_mask:0xf
	v_add_f32_dpp v16, v16, v16 row_half_mirror row_mask:0xf bank_mask:0xf
	v_add_f32_dpp v17, v17, v17 row_half_mirror row_mask:0xf bank_mask:0xf
	v_add_f32_dpp v18, v18, v18 row_half_mirror row_mask:0xf bank_mask:0xf
	v_add_f32_dpp v19, v19, v19 row_half_mirror row_mask:0xf bank_mask:0xf
	v_add_f32_dpp v20, v20, v20 row_half_mirror row_mask:0xf bank_mask:0xf
	v_add_f32_dpp v21, v21, v21 row_half_mirror row_mask:0xf bank_mask:0xf
	v_add_f32_dpp v14, v14, v14 row_mirror row_mask:0xf bank_mask:0xf
	v_add_f32_dpp v15, v15, v15 row_mirror row_mask:0xf bank_mask:0xf
	v_add_f32_dpp v16, v16, v16 row_mirror row_mask:0xf bank_mask:0xf
	v_add_f32_dpp v17, v17, v17 row_mirror row_mask:0xf bank_mask:0xf
	v_add_f32_dpp v18, v18, v18 row_mirror row_mask:0xf bank_mask:0xf
	v_add_f32_dpp v19, v19, v19 row_mirror row_mask:0xf bank_mask:0xf
	v_add_f32_dpp v20, v20, v20 row_mirror row_mask:0xf bank_mask:0xf
	v_add_f32_dpp v21, v21, v21 row_mirror row_mask:0xf bank_mask:0xf
	ds_bpermute_b32 v22, v181, v14
	ds_bpermute_b32 v23, v181, v15
	ds_bpermute_b32 v24, v181, v16
	ds_bpermute_b32 v25, v181, v17
	ds_bpermute_b32 v26, v181, v18
	ds_bpermute_b32 v27, v181, v19
	ds_bpermute_b32 v28, v181, v20
	ds_bpermute_b32 v29, v181, v21
	s_waitcnt lgkmcnt(0)
	v_pk_add_f32 v[14:15], v[14:15], v[22:23]
	v_pk_add_f32 v[16:17], v[16:17], v[24:25]
	v_pk_add_f32 v[18:19], v[18:19], v[26:27]
	v_pk_add_f32 v[20:21], v[20:21], v[28:29]
	ds_bpermute_b32 v22, v183, v14
	ds_bpermute_b32 v23, v183, v15
	ds_bpermute_b32 v24, v183, v16
	ds_bpermute_b32 v25, v183, v17
	ds_bpermute_b32 v26, v183, v18
	ds_bpermute_b32 v27, v183, v19
	ds_bpermute_b32 v28, v183, v20
	ds_bpermute_b32 v29, v183, v21
	s_waitcnt lgkmcnt(0)
	v_pk_add_f32 v[14:15], v[14:15], v[22:23]
	v_pk_add_f32 v[16:17], v[16:17], v[24:25]
	v_pk_add_f32 v[18:19], v[18:19], v[26:27]
	v_pk_add_f32 v[20:21], v[20:21], v[28:29]
	s_and_saveexec_b64 s[4:5], vcc
	s_cbranch_execz .LBB5_2
	v_lshrrev_b32_e32 v22, 1, v0
	v_add_u32_e32 v22, 0x20000, v22
	ds_write_b128 v22, v[14:17]
	ds_write_b128 v22, v[18:21] offset:16

.LBB5_8:
	s_or_b64 exec, exec, s[38:39]
	v_add_u32_e32 v156, 0x8000, v142
	s_load_dwordx2 s[38:39], s[0:1], 0x78
	s_load_dwordx2 s[44:45], s[0:1], 0x68
	s_load_dwordx2 s[48:49], s[0:1], 0x28
	s_mov_b64 s[0:1], 0x80
	v_readfirstlane_b32 s61, v156
	v_add_u32_e32 v157, 0xa000, v142
	v_lshl_add_u64 v[10:11], v[10:11], 0, s[0:1]
	s_mov_b32 m0, s61
	v_readfirstlane_b32 s61, v157
	s_waitcnt vmcnt(2)
	s_barrier
	s_mov_b32 m0, s61
	s_add_i32 s61, 0, 0x18000
	v_add_u32_e32 v158, s61, v162
	v_lshl_add_u64 v[8:9], v[8:9], 0, s[0:1]
	v_readfirstlane_b32 s62, v158
	s_add_u32 s56, s56, 0x80080
	s_mov_b32 m0, s62
	v_add_u32_e32 v159, 0x2000, v158
	s_addc_u32 s57, s57, 0
	s_add_i32 s62, 0, 0x1c000
	v_lshl_add_u64 v[6:7], v[6:7], 0, s[0:1]
	v_lshl_add_u64 v[4:5], v[4:5], 0, s[0:1]
	v_readfirstlane_b32 s0, v159
	v_add_u32_e32 v160, s62, v162
	global_load_lds_dwordx4 v[6:7], off
	s_mov_b32 m0, s0
	v_readfirstlane_b32 s63, v160
	v_add_u32_e32 v161, 0x2000, v160
	global_load_lds_dwordx4 v[4:5], off
	s_mov_b32 m0, s63
	v_readfirstlane_b32 s63, v161
	global_load_lds_dwordx4 v130, s[56:57]
	s_mov_b32 m0, s63
	v_lshlrev_b32_e32 v4, 6, v0
	global_load_lds_dwordx4 v132, s[56:57]
	v_lshlrev_b32_e32 v185, 2, v0
	v_and_b32_e32 v146, 48, v0
	v_and_b32_e32 v5, 0x3c0, v4
	v_and_b32_e32 v152, 32, v185
	v_bitop3_b32 v5, v5, v152, v146 bitop3:0x36
	s_add_u32 s3, s54, s3
	v_add_u32_e32 v8, s35, v5
	s_addc_u32 s35, s55, 0
	s_add_u32 s30, s30, s3
	s_addc_u32 s31, s31, s35
	s_lshl_b32 s2, s2, 16
	v_and_b32_e32 v15, 0x3000, v4
	v_add_u16_e32 v4, v12, v13
	s_and_b32 s2, s2, 0x300000
	v_lshrrev_b16_e32 v6, 1, v4
	v_lshlrev_b32_e32 v4, 8, v0
	v_lshlrev_b32_e32 v7, 4, v164
	s_add_u32 s2, s52, s2
	v_and_b32_e32 v4, 0x18000, v4
	v_lshlrev_b32_e32 v3, 11, v3
	v_and_b32_e32 v7, 0x38000, v7
	s_addc_u32 s3, s53, 0
	s_waitcnt vmcnt(4)
	v_lshlrev_b32_e32 v14, 13, v14
	v_or3_b32 v4, v6, v4, v3
	v_or3_b32 v3, v6, v7, v3
	s_add_u32 s2, s28, s2
	v_add_u32_e32 v9, s60, v5
	v_add_u32_e32 v10, s61, v5
	v_add_u32_e32 v11, s62, v5
	v_add_u32_e32 v16, 0, v5
	v_or_b32_e32 v17, 0x800, v14
	v_or_b32_e32 v18, 0x1000, v14
	v_or_b32_e32 v19, 0x1800, v14
	v_lshlrev_b32_e32 v4, 1, v4
	v_mov_b32_e32 v5, v2
	v_lshlrev_b32_e32 v6, 1, v3
	v_mov_b32_e32 v7, v2
	s_addc_u32 s3, s29, s3
	s_mov_b64 s[0:1], 0x80080
	v_lshl_add_u64 v[134:135], s[30:31], 0, v[4:5]
	v_lshl_add_u64 v[136:137], s[30:31], 0, v[6:7]
	v_lshl_add_u64 v[138:139], s[2:3], 0, v[4:5]
	v_lshl_add_u64 v[140:141], s[2:3], 0, v[6:7]
	s_mov_b32 s35, -2
	s_mov_b64 s[2:3], 0
	v_add_u32_e32 v165, v8, v15
	v_add_u32_e32 v150, v16, v14
	v_add_u32_e32 v149, v16, v17
	v_add_u32_e32 v148, v16, v18
	v_add_u32_e32 v147, v16, v19
	v_add_u32_e32 v163, v9, v15
	s_mov_b64 s[28:29], 0x100
	s_mov_b64 s[30:31], 0x80100
	v_add_u32_e32 v133, v10, v15
	s_mov_b64 s[52:53], 0x180
	s_mov_b64 s[54:55], 0x80180
	v_add_u32_e32 v131, v11, v15
	v_mov_b32_e32 v3, v2
	v_mov_b32_e32 v4, v2
	v_mov_b32_e32 v6, v2
	v_mov_b32_e32 v8, v2
	v_mov_b32_e32 v9, v2
	v_mov_b32_e32 v10, v2
	v_mov_b32_e32 v11, v2
	v_mov_b32_e32 v12, v2
	v_mov_b32_e32 v13, v2
	v_mov_b32_e32 v14, v2
	v_mov_b32_e32 v15, v2
	v_mov_b32_e32 v16, v2
	v_mov_b32_e32 v17, v2
	v_mov_b32_e32 v18, v2
	v_mov_b32_e32 v19, v2
	v_mov_b32_e32 v20, v2
	v_mov_b32_e32 v21, v2
	v_mov_b32_e32 v22, v2
	v_mov_b32_e32 v23, v2
	v_mov_b32_e32 v24, v2
	v_mov_b32_e32 v25, v2
	v_mov_b32_e32 v26, v2
	v_mov_b32_e32 v27, v2
	v_mov_b32_e32 v28, v2
	v_mov_b32_e32 v29, v2
	v_mov_b32_e32 v30, v2
	v_mov_b32_e32 v31, v2
	v_mov_b32_e32 v32, v2
	v_mov_b32_e32 v33, v2
	v_mov_b32_e32 v34, v2
	v_mov_b32_e32 v35, v2
	v_mov_b32_e32 v36, v2
	v_mov_b32_e32 v37, v2
	v_mov_b32_e32 v38, v2
	v_mov_b32_e32 v39, v2
	v_mov_b32_e32 v40, v2
	v_mov_b32_e32 v41, v2
	v_mov_b32_e32 v42, v2
	v_mov_b32_e32 v43, v2
	v_mov_b32_e32 v44, v2
	v_mov_b32_e32 v45, v2
	v_mov_b32_e32 v46, v2
	v_mov_b32_e32 v47, v2
	v_mov_b32_e32 v48, v2
	v_mov_b32_e32 v49, v2
	v_mov_b32_e32 v50, v2
	v_mov_b32_e32 v51, v2
	v_mov_b32_e32 v52, v2
	v_mov_b32_e32 v53, v2
	v_mov_b32_e32 v54, v2
	v_mov_b32_e32 v55, v2
	v_mov_b32_e32 v56, v2
	v_mov_b32_e32 v57, v2
	v_mov_b32_e32 v58, v2
	v_mov_b32_e32 v59, v2
	v_mov_b32_e32 v60, v2
	v_mov_b32_e32 v61, v2
	v_mov_b32_e32 v62, v2
	v_mov_b32_e32 v63, v2
	v_mov_b32_e32 v64, v2
	v_mov_b32_e32 v65, v2
	v_mov_b32_e32 v66, v2
	v_mov_b32_e32 v67, v2
	v_mov_b32_e32 v68, v2
	v_mov_b32_e32 v69, v2
	v_mov_b32_e32 v70, v2
	v_mov_b32_e32 v71, v2
	v_mov_b32_e32 v72, v2
	v_mov_b32_e32 v73, v2
	v_mov_b32_e32 v74, v2
	v_mov_b32_e32 v75, v2
	v_mov_b32_e32 v76, v2
	v_mov_b32_e32 v77, v2
	v_mov_b32_e32 v78, v2
	v_mov_b32_e32 v79, v2
	v_mov_b32_e32 v80, v2
	v_mov_b32_e32 v81, v2
	v_mov_b32_e32 v82, v2
	v_mov_b32_e32 v83, v2
	v_mov_b32_e32 v84, v2
	v_mov_b32_e32 v85, v2
	v_mov_b32_e32 v86, v2
	v_mov_b32_e32 v87, v2
	v_mov_b32_e32 v88, v2
	v_mov_b32_e32 v89, v2
	v_mov_b32_e32 v90, v2
	v_mov_b32_e32 v91, v2
	v_mov_b32_e32 v92, v2
	v_mov_b32_e32 v93, v2
	v_mov_b32_e32 v94, v2
	v_mov_b32_e32 v95, v2
	v_mov_b32_e32 v96, v2
	v_mov_b32_e32 v97, v2
	v_mov_b32_e32 v98, v2
	v_mov_b32_e32 v99, v2
	v_mov_b32_e32 v100, v2
	v_mov_b32_e32 v101, v2
	v_mov_b32_e32 v102, v2
	v_mov_b32_e32 v103, v2
	v_mov_b32_e32 v104, v2
	v_mov_b32_e32 v105, v2
	v_mov_b32_e32 v106, v2
	v_mov_b32_e32 v107, v2
	v_mov_b32_e32 v108, v2
	v_mov_b32_e32 v109, v2
	v_mov_b32_e32 v110, v2
	v_mov_b32_e32 v111, v2
	v_mov_b32_e32 v112, v2
	v_mov_b32_e32 v113, v2
	v_mov_b32_e32 v114, v2
	v_mov_b32_e32 v115, v2
	v_mov_b32_e32 v116, v2
	v_mov_b32_e32 v117, v2
	v_mov_b32_e32 v118, v2
	v_mov_b32_e32 v119, v2
	v_mov_b32_e32 v120, v2
	v_mov_b32_e32 v121, v2
	v_mov_b32_e32 v122, v2
	v_mov_b32_e32 v123, v2
	v_mov_b32_e32 v124, v2
	v_mov_b32_e32 v125, v2
	v_mov_b32_e32 v126, v2
	v_mov_b32_e32 v127, v2
	v_mov_b32_e32 v128, v2
	v_mov_b32_e32 v129, v2
	v_lshrrev_b32_e32 v190, 2, v0
	v_and_b32_e32 v186, 48, v162
	v_and_b32_e32 v188, 15, v0
	v_add_u32_e32 v166, 0xc000, v142
	v_add_u32_e32 v167, 0xe000, v142
	s_barrier
